# gate/up fp8 K-loop body: phase-2 LDS-DMA tile loads issued one MMA segment earlier (interleaved with phase-1 MFMAs); vmcnt order unchanged
# baseline (speedup 1.0000x reference)
.LBB0_249:
	s_add_u32 s4, s46, s26
	s_addc_u32 s36, s47, s27
	s_add_u32 s69, s4, 0x2e000100
	s_addc_u32 s70, s36, 0
	s_add_u32 s74, s61, s26
	s_addc_u32 s86, s63, s27
	s_add_i32 s4, 0, 0x10000
	s_cmpk_eq_i32 s26, 0x300
	s_cselect_b64 vcc, -1, 0
	s_and_b64 s[36:37], vcc, exec
	s_cselect_b32 s71, s41, s70
	s_cselect_b32 s70, s40, s69
	v_add_u32_e32 v0, s4, v200
	s_cselect_b32 s37, s6, s86
	s_cselect_b32 s36, s31, s74
	s_add_i32 s69, 0, 0x14000
	ds_read_b128 v[18:21], v0
	ds_read_b128 v[22:25], v0 offset:1024
	ds_read_b128 v[26:29], v0 offset:2048
	ds_read_b128 v[30:33], v0 offset:3072
	v_add_u32_e32 v0, s69, v200
	ds_read_b128 v[2:5], v0
	ds_read_b128 v[6:9], v0 offset:1024
	ds_read_b128 v[10:13], v0 offset:2048
	ds_read_b128 v[14:17], v0 offset:3072
	v_lshl_add_u64 v[222:223], v[178:179], 0, s[26:27]
	s_add_i32 m0, s93, 0xc000
	ds_read_b128 v[180:183], v201
	ds_read_b128 v[184:187], v201 offset:1024
	ds_read_b128 v[206:209], v201 offset:2048
	ds_read_b128 v[210:213], v201 offset:3072
	ds_read_b128 v[214:217], v201 offset:4096
	ds_read_b128 v[218:221], v201 offset:5120
	ds_read_b128 v[234:237], v201 offset:6144
	ds_read_b128 v[238:241], v201 offset:7168
	global_load_lds_dwordx4 v[222:223], off
	v_lshl_add_u64 v[222:223], v[176:177], 0, s[26:27]
	s_add_i32 m0, s93, 0xe000
	s_nop 0
	global_load_lds_dwordx4 v[222:223], off
	s_waitcnt vmcnt(8)
	s_waitcnt lgkmcnt(0)
	s_barrier
	s_setprio 1
	s_waitcnt lgkmcnt(0)
	v_mfma_f32_16x16x128_f8f6f4 v[158:161], v[18:25], v[180:187], v[158:161]
	v_mfma_f32_16x16x128_f8f6f4 v[154:157], v[26:33], v[180:187], v[154:157]
	v_mfma_f32_16x16x128_f8f6f4 v[142:145], v[18:25], v[206:213], v[142:145]
	v_mfma_f32_16x16x128_f8f6f4 v[138:141], v[26:33], v[206:213], v[138:141]
	v_mfma_f32_16x16x128_f8f6f4 v[126:129], v[18:25], v[214:221], v[126:129]
	v_mfma_f32_16x16x128_f8f6f4 v[122:125], v[26:33], v[214:221], v[122:125]
	v_mfma_f32_16x16x128_f8f6f4 v[110:113], v[18:25], v[234:241], v[110:113]
	v_mfma_f32_16x16x128_f8f6f4 v[106:109], v[26:33], v[234:241], v[106:109]
	s_setprio 0
	s_setprio 1
	v_mfma_f32_16x16x128_f8f6f4 v[150:153], v[2:9], v[180:187], v[150:153]
	s_add_i32 s100, s4, s92
	v_lshl_add_u64 v[242:243], s[36:37], 0, v[162:163]
	s_mov_b32 m0, s100
	v_mfma_f32_16x16x128_f8f6f4 v[146:149], v[10:17], v[180:187], v[146:149]
	global_load_lds_dwordx4 v[242:243], off
	s_add_i32 m0, s100, 0x2000
	v_lshl_add_u64 v[244:245], s[36:37], 0, v[164:165]
	s_add_u32 s86, s36, 0x20000
	v_mfma_f32_16x16x128_f8f6f4 v[134:137], v[2:9], v[206:213], v[134:137]
	global_load_lds_dwordx4 v[244:245], off
	s_addc_u32 s87, s37, 0
	s_add_i32 s101, s69, s92
	v_mfma_f32_16x16x128_f8f6f4 v[130:133], v[10:17], v[206:213], v[130:133]
	v_lshl_add_u64 v[246:247], s[86:87], 0, v[162:163]
	s_mov_b32 m0, s101
	v_lshl_add_u64 v[244:245], s[86:87], 0, v[164:165]
	v_mfma_f32_16x16x128_f8f6f4 v[118:121], v[2:9], v[214:221], v[118:121]
	global_load_lds_dwordx4 v[246:247], off
	s_add_i32 m0, s101, 0x2000
	v_cndmask_b32_e32 v248, v168, v202, vcc
	v_mfma_f32_16x16x128_f8f6f4 v[114:117], v[10:17], v[214:221], v[114:117]
	global_load_lds_dwordx4 v[244:245], off
	s_mov_b32 m0, s93
	v_cndmask_b32_e32 v249, v170, v203, vcc
	v_mfma_f32_16x16x128_f8f6f4 v[102:105], v[2:9], v[234:241], v[102:105]
	global_load_lds_dwordx4 v248, s[70:71]
	s_mov_b32 m0, s79
	v_mfma_f32_16x16x128_f8f6f4 v[98:101], v[10:17], v[234:241], v[98:101]
	global_load_lds_dwordx4 v249, s[70:71]
	s_setprio 0
	s_barrier
	s_add_i32 s4, s4, s92
	v_lshl_add_u64 v[180:181], s[36:37], 0, v[162:163]
	s_mov_b32 m0, s4
	ds_read_b128 v[206:209], v201 offset:16384
	ds_read_b128 v[210:213], v201 offset:17408
	ds_read_b128 v[214:217], v201 offset:18432
	ds_read_b128 v[218:221], v201 offset:19456
	ds_read_b128 v[234:237], v201 offset:20480
	ds_read_b128 v[238:241], v201 offset:21504
	ds_read_b128 v[242:245], v201 offset:22528
	ds_read_b128 v[246:249], v201 offset:23552
	s_add_i32 m0, s4, 0x2000
	s_add_u32 s86, s36, 0x20000
	v_lshl_add_u64 v[182:183], s[36:37], 0, v[164:165]
	s_addc_u32 s87, s37, 0
	s_add_i32 s4, s69, s92
	v_lshl_add_u64 v[184:185], s[86:87], 0, v[162:163]
	s_mov_b32 m0, s4
	v_cndmask_b32_e32 v0, v168, v202, vcc
	v_lshl_add_u64 v[184:185], s[86:87], 0, v[164:165]
	s_add_i32 m0, s4, 0x2000
	v_lshl_add_u64 v[186:187], s[70:71], 0, v[0:1]
	s_mov_b32 m0, s93
	v_cndmask_b32_e32 v184, v170, v203, vcc
	s_mov_b32 m0, s79
	v_mov_b32_e32 v185, v1
	s_waitcnt vmcnt(8)
	s_waitcnt lgkmcnt(0)
	v_lshl_add_u64 v[184:185], s[70:71], 0, v[184:185]
	s_barrier
	s_setprio 1
	s_waitcnt lgkmcnt(0)
	v_mfma_f32_16x16x128_f8f6f4 v[94:97], v[18:25], v[206:213], v[94:97]
	v_mfma_f32_16x16x128_f8f6f4 v[90:93], v[26:33], v[206:213], v[90:93]
	v_mfma_f32_16x16x128_f8f6f4 v[70:73], v[18:25], v[214:221], v[70:73]
	v_mfma_f32_16x16x128_f8f6f4 v[66:69], v[26:33], v[214:221], v[66:69]
	v_mfma_f32_16x16x128_f8f6f4 v[54:57], v[18:25], v[234:241], v[54:57]
	v_mfma_f32_16x16x128_f8f6f4 v[50:53], v[26:33], v[234:241], v[50:53]
	v_mfma_f32_16x16x128_f8f6f4 v[38:41], v[18:25], v[242:249], v[38:41]
	v_mfma_f32_16x16x128_f8f6f4 v[34:37], v[26:33], v[242:249], v[34:37]
	s_setprio 0
	s_setprio 1
	v_mfma_f32_16x16x128_f8f6f4 v[86:89], v[2:9], v[206:213], v[86:89]
	v_mfma_f32_16x16x128_f8f6f4 v[82:85], v[10:17], v[206:213], v[82:85]
	v_mfma_f32_16x16x128_f8f6f4 v[78:81], v[2:9], v[214:221], v[78:81]
	v_mfma_f32_16x16x128_f8f6f4 v[74:77], v[10:17], v[214:221], v[74:77]
	v_mfma_f32_16x16x128_f8f6f4 v[62:65], v[2:9], v[234:241], v[62:65]
	v_mfma_f32_16x16x128_f8f6f4 v[58:61], v[10:17], v[234:241], v[58:61]
	v_mfma_f32_16x16x128_f8f6f4 v[46:49], v[2:9], v[242:249], v[46:49]
	v_mfma_f32_16x16x128_f8f6f4 v[42:45], v[10:17], v[242:249], v[42:45]
	s_setprio 0
	s_barrier
	s_add_i32 s4, 0, 0x18000
	v_add_u32_e32 v0, s4, v200
	s_add_i32 s69, 0, 0x1c000
	ds_read_b128 v[2:5], v0
	ds_read_b128 v[6:9], v0 offset:1024
	ds_read_b128 v[10:13], v0 offset:2048
	ds_read_b128 v[14:17], v0 offset:3072
	v_add_u32_e32 v0, s69, v200
	ds_read_b128 v[18:21], v0
	ds_read_b128 v[22:25], v0 offset:1024
	ds_read_b128 v[26:29], v0 offset:2048
	ds_read_b128 v[30:33], v0 offset:3072
	s_mov_b32 m0, s84
	v_cndmask_b32_e32 v0, v172, v204, vcc
	ds_read_b128 v[206:209], v201 offset:32768
	ds_read_b128 v[210:213], v201 offset:33792
	ds_read_b128 v[214:217], v201 offset:34816
	ds_read_b128 v[218:221], v201 offset:35840
	ds_read_b128 v[234:237], v201 offset:36864
	ds_read_b128 v[238:241], v201 offset:37888
	ds_read_b128 v[242:245], v201 offset:38912
	ds_read_b128 v[246:249], v201 offset:39936
	v_cndmask_b32_e32 v173, v174, v205, vcc
	global_load_lds_dwordx4 v0, s[70:71]
	s_mov_b32 m0, s85
	s_nop 0
	global_load_lds_dwordx4 v173, s[70:71]
	s_waitcnt vmcnt(8)
	s_waitcnt lgkmcnt(0)
	s_barrier
	s_setprio 1
	s_waitcnt lgkmcnt(0)
	v_mfma_f32_16x16x128_f8f6f4 v[158:161], v[2:9], v[206:213], v[158:161]
	v_mfma_f32_16x16x128_f8f6f4 v[154:157], v[10:17], v[206:213], v[154:157]
	v_mfma_f32_16x16x128_f8f6f4 v[142:145], v[2:9], v[214:221], v[142:145]
	v_mfma_f32_16x16x128_f8f6f4 v[138:141], v[10:17], v[214:221], v[138:141]
	v_mfma_f32_16x16x128_f8f6f4 v[126:129], v[2:9], v[234:241], v[126:129]
	v_mfma_f32_16x16x128_f8f6f4 v[122:125], v[10:17], v[234:241], v[122:125]
	v_mfma_f32_16x16x128_f8f6f4 v[110:113], v[2:9], v[242:249], v[110:113]
	v_mfma_f32_16x16x128_f8f6f4 v[106:109], v[10:17], v[242:249], v[106:109]
	s_setprio 0
	s_setprio 1
	v_mfma_f32_16x16x128_f8f6f4 v[150:153], v[18:25], v[206:213], v[150:153]
	v_mfma_f32_16x16x128_f8f6f4 v[146:149], v[26:33], v[206:213], v[146:149]
	v_mfma_f32_16x16x128_f8f6f4 v[134:137], v[18:25], v[214:221], v[134:137]
	v_mfma_f32_16x16x128_f8f6f4 v[130:133], v[26:33], v[214:221], v[130:133]
	v_mfma_f32_16x16x128_f8f6f4 v[118:121], v[18:25], v[234:241], v[118:121]
	v_mfma_f32_16x16x128_f8f6f4 v[114:117], v[26:33], v[234:241], v[114:117]
	v_mfma_f32_16x16x128_f8f6f4 v[102:105], v[18:25], v[242:249], v[102:105]
	v_mfma_f32_16x16x128_f8f6f4 v[98:101], v[26:33], v[242:249], v[98:101]
	s_setprio 0
	s_barrier
	s_add_i32 s4, s4, s92
	v_lshl_add_u64 v[180:181], v[180:181], 0, s[22:23]
	s_mov_b32 m0, s4
	ds_read_b128 v[206:209], v201 offset:49152
	ds_read_b128 v[210:213], v201 offset:50176
	ds_read_b128 v[214:217], v201 offset:51200
	ds_read_b128 v[218:221], v201 offset:52224
	ds_read_b128 v[234:237], v201 offset:53248
	ds_read_b128 v[238:241], v201 offset:54272
	ds_read_b128 v[242:245], v201 offset:55296
	ds_read_b128 v[246:249], v201 offset:56320
	global_load_lds_dwordx4 v[180:181], off
	s_add_i32 m0, s4, 0x2000
	s_add_u32 s36, s36, 0x20080
	v_lshl_add_u64 v[180:181], v[182:183], 0, s[22:23]
	s_addc_u32 s37, s37, 0
	s_add_i32 s4, s69, s92
	global_load_lds_dwordx4 v[180:181], off
	v_lshl_add_u64 v[180:181], s[36:37], 0, v[162:163]
	s_mov_b32 m0, s4
	s_nop 0
	global_load_lds_dwordx4 v[180:181], off
	v_lshl_add_u64 v[180:181], s[36:37], 0, v[164:165]
	s_add_i32 m0, s4, 0x2000
	s_nop 0
	global_load_lds_dwordx4 v[180:181], off
	v_lshl_add_u64 v[180:181], v[186:187], 0, s[22:23]
	s_mov_b32 m0, s15
	s_nop 0
	global_load_lds_dwordx4 v[180:181], off
	v_lshl_add_u64 v[180:181], v[184:185], 0, s[22:23]
	s_mov_b32 m0, s16
	s_nop 0
	global_load_lds_dwordx4 v[180:181], off
	s_waitcnt vmcnt(8)
	s_waitcnt lgkmcnt(0)
	s_barrier
	s_setprio 1
	s_waitcnt lgkmcnt(0)
	v_mfma_f32_16x16x128_f8f6f4 v[94:97], v[2:9], v[206:213], v[94:97]
	v_mfma_f32_16x16x128_f8f6f4 v[90:93], v[10:17], v[206:213], v[90:93]
	v_mfma_f32_16x16x128_f8f6f4 v[70:73], v[2:9], v[214:221], v[70:73]
	v_mfma_f32_16x16x128_f8f6f4 v[66:69], v[10:17], v[214:221], v[66:69]
	v_mfma_f32_16x16x128_f8f6f4 v[54:57], v[2:9], v[234:241], v[54:57]
	v_mfma_f32_16x16x128_f8f6f4 v[50:53], v[10:17], v[234:241], v[50:53]
	v_mfma_f32_16x16x128_f8f6f4 v[38:41], v[2:9], v[242:249], v[38:41]
	v_mfma_f32_16x16x128_f8f6f4 v[34:37], v[10:17], v[242:249], v[34:37]
	s_setprio 0
	s_setprio 1
	v_mfma_f32_16x16x128_f8f6f4 v[86:89], v[18:25], v[206:213], v[86:89]
	v_mfma_f32_16x16x128_f8f6f4 v[82:85], v[26:33], v[206:213], v[82:85]
	v_mfma_f32_16x16x128_f8f6f4 v[78:81], v[18:25], v[214:221], v[78:81]
	v_mfma_f32_16x16x128_f8f6f4 v[74:77], v[26:33], v[214:221], v[74:77]
	v_mfma_f32_16x16x128_f8f6f4 v[62:65], v[18:25], v[234:241], v[62:65]
	v_mfma_f32_16x16x128_f8f6f4 v[58:61], v[26:33], v[234:241], v[58:61]
	v_mfma_f32_16x16x128_f8f6f4 v[46:49], v[18:25], v[242:249], v[46:49]
	v_mfma_f32_16x16x128_f8f6f4 v[42:45], v[26:33], v[242:249], v[42:45]
	s_setprio 0
	s_barrier
	s_add_i32 s67, s67, 2
	s_add_u32 s26, s26, 0x100
	s_addc_u32 s27, s27, 0
	s_cmp_gt_u32 s67, 5
	s_cbranch_scc0 .LBB0_249
	s_ashr_i32 s69, s68, 31
	s_lshl_b32 s66, s66, 7
	s_lshl_b64 s[26:27], s[68:69], 13
	v_or_b32_e32 v2, s66, v169
	s_add_u32 s26, s5, s26
	s_addc_u32 s27, s14, s27
	v_ashrrev_i32_e32 v3, 31, v2
	v_lshl_add_u64 v[6:7], v[2:3], 2, s[26:27]
	s_mov_b64 s[26:27], 0x1000
	v_lshl_add_u64 v[14:15], v[6:7], 0, s[26:27]
	ds_read_b128 v[2:5], v233 offset:64
	ds_read_b128 v[10:13], v233
	v_add_co_u32_e32 v6, vcc, s9, v6
	v_lshl_add_u32 v22, s75, 8, v171
	s_nop 0
	v_addc_co_u32_e32 v7, vcc, 0, v7, vcc
	ds_read_b128 v[6:9], v233 offset:128
	s_nop 0
	ds_read_b128 v[14:17], v233 offset:192
	s_and_b64 vcc, exec, s[58:59]
	s_cbranch_vccz .LBB0_252
	s_barrier
